# adj stream by LDS-DMA (buffer_load lds) into a 20-slot per-wave LDS ring, pieces read back with ds_read_b128 one ahead
# baseline (speedup 1.0000x reference)
_Z11attn_kernelPKfS0_PKDv8_DF16_S0_Pfi:
	s_load_dwordx2 s[28:29], s[0:1], 0x0
	v_cmp_gt_u32_e32 vcc, 8, v0
	s_and_saveexec_b64 s[4:5], vcc
	v_lshlrev_b32_e32 v1, 2, v0
	v_mov_b32_e32 v2, 0
	ds_write_b32 v1, v2 offset:36864
	s_or_b64 exec, exec, s[4:5]
	s_load_dword s33, s[0:1], 0x28
	v_bfe_u32 v1, v0, 6, 2
	v_lshl_or_b32 v82, s2, 2, v1
	v_readfirstlane_b32 s34, v0
	s_cmp_gt_u32 s34, 0xff
	s_cbranch_scc1 .Lsc_early_skip
	v_and_b32_e32 v3, 63, v0
	v_lshlrev_b32_e32 v2, 4, v3
	s_lshr_b32 s35, s34, 6
	s_lshl_b32 s37, s2, 2
	s_add_u32 s37, s37, s35
	s_and_b32 s47, s37, 1
	s_lshl_b32 s47, s47, 2
	s_mul_i32 s38, s37, 0x9c40
	s_lshl_b32 s40, s47, 4
	s_sub_u32 s38, s38, s40
	v_max_u32_e32 v12, s47, v3
	v_lshlrev_b32_e32 v12, 4, v12
	s_mul_i32 s6, s35, 0x5000
	s_add_u32 s6, s6, 0x9400
	s_waitcnt lgkmcnt(0)
	s_and_b32 s29, s29, 0xffff
	s_mov_b32 s30, 0x17d78400
	s_mov_b32 s31, 0x20000
	s_mov_b32 m0, s6
	s_mov_b32 s40, s38
	buffer_load_dwordx4 v12, s[28:31], s40 offen nt lds
	s_add_u32 m0, s6, 0x400
	s_add_u32 s40, s38, 0x400
	buffer_load_dwordx4 v2, s[28:31], s40 offen nt lds
	s_add_u32 m0, s6, 0x800
	s_add_u32 s40, s38, 0x800
	buffer_load_dwordx4 v2, s[28:31], s40 offen nt lds
	s_add_u32 m0, s6, 0xc00
	s_add_u32 s40, s38, 0xc00
	buffer_load_dwordx4 v2, s[28:31], s40 offen nt lds
	s_add_u32 m0, s6, 0x1000
	s_add_u32 s40, s38, 0x1000
	buffer_load_dwordx4 v2, s[28:31], s40 offen nt lds
	s_add_u32 m0, s6, 0x1400
	s_add_u32 s40, s38, 0x1400
	buffer_load_dwordx4 v2, s[28:31], s40 offen nt lds
	s_add_u32 m0, s6, 0x1800
	s_add_u32 s40, s38, 0x1800
	buffer_load_dwordx4 v2, s[28:31], s40 offen nt lds
	s_add_u32 m0, s6, 0x1c00
	s_add_u32 s40, s38, 0x1c00
	buffer_load_dwordx4 v2, s[28:31], s40 offen nt lds
	s_add_u32 m0, s6, 0x2000
	s_add_u32 s40, s38, 0x2000
	buffer_load_dwordx4 v2, s[28:31], s40 offen nt lds
	s_add_u32 m0, s6, 0x2400
	s_add_u32 s40, s38, 0x2400
	buffer_load_dwordx4 v2, s[28:31], s40 offen nt lds
	s_add_u32 m0, s6, 0x2800
	s_add_u32 s40, s38, 0x2800
	buffer_load_dwordx4 v2, s[28:31], s40 offen nt lds
	s_add_u32 m0, s6, 0x2c00
	s_add_u32 s40, s38, 0x2c00
	buffer_load_dwordx4 v2, s[28:31], s40 offen nt lds
	s_add_u32 m0, s6, 0x3000
	s_add_u32 s40, s38, 0x3000
	buffer_load_dwordx4 v2, s[28:31], s40 offen nt lds
	s_add_u32 m0, s6, 0x3400
	s_add_u32 s40, s38, 0x3400
	buffer_load_dwordx4 v2, s[28:31], s40 offen nt lds
	s_add_u32 m0, s6, 0x3800
	s_add_u32 s40, s38, 0x3800
	buffer_load_dwordx4 v2, s[28:31], s40 offen nt lds
	s_add_u32 m0, s6, 0x3c00
	s_add_u32 s40, s38, 0x3c00
	buffer_load_dwordx4 v2, s[28:31], s40 offen nt lds
	s_add_u32 m0, s6, 0x4000
	s_add_u32 s40, s38, 0x4000
	buffer_load_dwordx4 v2, s[28:31], s40 offen nt lds
	s_add_u32 m0, s6, 0x4400
	s_add_u32 s40, s38, 0x4400
	buffer_load_dwordx4 v2, s[28:31], s40 offen nt lds
	s_add_u32 m0, s6, 0x4800
	s_add_u32 s40, s38, 0x4800
	buffer_load_dwordx4 v2, s[28:31], s40 offen nt lds
	s_add_u32 m0, s6, 0x4c00
	s_add_u32 s40, s38, 0x4c00
	buffer_load_dwordx4 v2, s[28:31], s40 offen nt lds

.LBB1_217:
	s_andn2_saveexec_b64 s[0:1], s[30:31]
	s_cbranch_execz .LBB1_384
	v_readfirstlane_b32 s34, v1
	v_readfirstlane_b32 s37, v82
	v_readfirstlane_b32 s36, v84
	v_and_b32_e32 v3, 63, v0
	v_lshlrev_b32_e32 v2, 4, v3
	s_cmp_lt_i32 s36, 0
	s_cbranch_scc1 .LBB1_384
	s_waitcnt lgkmcnt(0)
	s_and_b32 s29, s29, 0xffff
	s_mov_b32 s30, 0x17d78400
	s_mov_b32 s31, 0x20000
	s_mov_b32 s35, 0
	s_movk_i32 s7, 0x80
	s_mov_b32 s9, 0x7fffffff
	s_lshl_b32 s44, s34, 12
	s_add_u32 s44, s44, 0x4000
	s_lshl_b32 s45, s34, 10
	s_add_u32 s45, s45, 0x8000
	s_lshl_b32 s46, s34, 3
	s_add_u32 s46, s46, 0x9000
	s_mul_i32 s6, s34, 0x5000
	s_add_u32 s6, s6, 0x9400
	v_add_u32_e32 v24, s6, v2
	s_and_b32 s47, s37, 1
	s_lshl_b32 s47, s47, 2
	s_mul_i32 s38, s37, 0x9c40
	s_lshl_b32 s40, s47, 4
	s_sub_u32 s38, s38, s40
	v_max_u32_e32 v12, s47, v3
	v_lshlrev_b32_e32 v12, 4, v12
	s_waitcnt vmcnt(19)
	ds_read_b128 v[16:19], v24

.Lsc_go:
	s_mov_b32 s42, 0
	s_waitcnt lgkmcnt(0)
	s_mov_b32 m0, s6
	s_add_u32 s40, s38, 0x5000
	buffer_load_dwordx4 v2, s[28:31], s40 offen nt lds
	s_waitcnt vmcnt(19)
	ds_read_b128 v[20:23], v24 offset:1024
	v_or3_b32 v12, v16, v17, v18
	v_bitop3_b32 v12, v12, s9, v19 bitop3:0xc8
	v_cmp_ne_u32_e32 vcc, 0, v12
	s_and_b64 vcc, vcc, s[48:49]
	s_cbranch_vccz .Lsc_s0
	s_nop 0
	v_mbcnt_lo_u32_b32 v13, vcc_lo, 0
	v_mbcnt_hi_u32_b32 v13, vcc_hi, v13
	v_add_u32_e32 v13, s42, v13
	v_cmp_gt_i32_e64 s[0:1], s7, v13
	s_and_b64 s[4:5], vcc, s[0:1]
	s_and_saveexec_b64 s[0:1], s[4:5]
	v_lshl_add_u32 v14, v13, 4, v9
	v_lshl_add_u32 v15, v13, 2, v10
	v_mov_b32_e32 v13, v8
	ds_write_b128 v14, v[16:19]
	ds_write_b32 v15, v13
	s_mov_b64 exec, -1
	s_bcnt1_i32_b64 s40, vcc
	s_add_i32 s42, s42, s40
.Lsc_s0:
	s_waitcnt lgkmcnt(0)
	s_add_u32 m0, s6, 0x400
	s_add_u32 s40, s38, 0x5400
	buffer_load_dwordx4 v2, s[28:31], s40 offen nt lds
	s_waitcnt vmcnt(19)
	ds_read_b128 v[16:19], v24 offset:2048
	v_or3_b32 v12, v20, v21, v22
	v_bitop3_b32 v12, v12, s9, v23 bitop3:0xc8
	v_cmp_ne_u32_e32 vcc, 0, v12
	s_cbranch_vccz .Lsc_s1
	s_nop 0
	v_mbcnt_lo_u32_b32 v13, vcc_lo, 0
	v_mbcnt_hi_u32_b32 v13, vcc_hi, v13
	v_add_u32_e32 v13, s42, v13
	v_cmp_gt_i32_e64 s[0:1], s7, v13
	s_and_b64 s[4:5], vcc, s[0:1]
	s_and_saveexec_b64 s[0:1], s[4:5]
	v_lshl_add_u32 v14, v13, 4, v9
	v_lshl_add_u32 v15, v13, 2, v10
	v_add_u32_e32 v13, 0x100, v8
	ds_write_b128 v14, v[20:23]
	ds_write_b32 v15, v13
	s_mov_b64 exec, -1
	s_bcnt1_i32_b64 s40, vcc
	s_add_i32 s42, s42, s40
.Lsc_s1:
	s_waitcnt lgkmcnt(0)
	s_add_u32 m0, s6, 0x800
	s_add_u32 s40, s38, 0x5800
	buffer_load_dwordx4 v2, s[28:31], s40 offen nt lds
	s_waitcnt vmcnt(19)
	ds_read_b128 v[20:23], v24 offset:3072
	v_or3_b32 v12, v16, v17, v18
	v_bitop3_b32 v12, v12, s9, v19 bitop3:0xc8
	v_cmp_ne_u32_e32 vcc, 0, v12
	s_cbranch_vccz .Lsc_s2
	s_nop 0
	v_mbcnt_lo_u32_b32 v13, vcc_lo, 0
	v_mbcnt_hi_u32_b32 v13, vcc_hi, v13
	v_add_u32_e32 v13, s42, v13
	v_cmp_gt_i32_e64 s[0:1], s7, v13
	s_and_b64 s[4:5], vcc, s[0:1]
	s_and_saveexec_b64 s[0:1], s[4:5]
	v_lshl_add_u32 v14, v13, 4, v9
	v_lshl_add_u32 v15, v13, 2, v10
	v_add_u32_e32 v13, 0x200, v8
	ds_write_b128 v14, v[16:19]
	ds_write_b32 v15, v13
	s_mov_b64 exec, -1
	s_bcnt1_i32_b64 s40, vcc
	s_add_i32 s42, s42, s40
.Lsc_s2:
	s_waitcnt lgkmcnt(0)
	s_add_u32 m0, s6, 0xc00
	s_add_u32 s40, s38, 0x5c00
	buffer_load_dwordx4 v2, s[28:31], s40 offen nt lds
	s_waitcnt vmcnt(19)
	ds_read_b128 v[16:19], v24 offset:4096
	v_or3_b32 v12, v20, v21, v22
	v_bitop3_b32 v12, v12, s9, v23 bitop3:0xc8
	v_cmp_ne_u32_e32 vcc, 0, v12
	s_cbranch_vccz .Lsc_s3
	s_nop 0
	v_mbcnt_lo_u32_b32 v13, vcc_lo, 0
	v_mbcnt_hi_u32_b32 v13, vcc_hi, v13
	v_add_u32_e32 v13, s42, v13
	v_cmp_gt_i32_e64 s[0:1], s7, v13
	s_and_b64 s[4:5], vcc, s[0:1]
	s_and_saveexec_b64 s[0:1], s[4:5]
	v_lshl_add_u32 v14, v13, 4, v9
	v_lshl_add_u32 v15, v13, 2, v10
	v_add_u32_e32 v13, 0x300, v8
	ds_write_b128 v14, v[20:23]
	ds_write_b32 v15, v13
	s_mov_b64 exec, -1
	s_bcnt1_i32_b64 s40, vcc
	s_add_i32 s42, s42, s40
.Lsc_s3:
	s_waitcnt lgkmcnt(0)
	s_add_u32 m0, s6, 0x1000
	s_add_u32 s40, s38, 0x6000
	buffer_load_dwordx4 v2, s[28:31], s40 offen nt lds
	s_waitcnt vmcnt(19)
	ds_read_b128 v[20:23], v24 offset:5120
	v_or3_b32 v12, v16, v17, v18
	v_bitop3_b32 v12, v12, s9, v19 bitop3:0xc8
	v_cmp_ne_u32_e32 vcc, 0, v12
	s_cbranch_vccz .Lsc_s4
	s_nop 0
	v_mbcnt_lo_u32_b32 v13, vcc_lo, 0
	v_mbcnt_hi_u32_b32 v13, vcc_hi, v13
	v_add_u32_e32 v13, s42, v13
	v_cmp_gt_i32_e64 s[0:1], s7, v13
	s_and_b64 s[4:5], vcc, s[0:1]
	s_and_saveexec_b64 s[0:1], s[4:5]
	v_lshl_add_u32 v14, v13, 4, v9
	v_lshl_add_u32 v15, v13, 2, v10
	v_add_u32_e32 v13, 0x400, v8
	ds_write_b128 v14, v[16:19]
	ds_write_b32 v15, v13
	s_mov_b64 exec, -1
	s_bcnt1_i32_b64 s40, vcc
	s_add_i32 s42, s42, s40
.Lsc_s4:
	s_waitcnt lgkmcnt(0)
	s_add_u32 m0, s6, 0x1400
	s_add_u32 s40, s38, 0x6400
	buffer_load_dwordx4 v2, s[28:31], s40 offen nt lds
	s_waitcnt vmcnt(19)
	ds_read_b128 v[16:19], v24 offset:6144
	v_or3_b32 v12, v20, v21, v22
	v_bitop3_b32 v12, v12, s9, v23 bitop3:0xc8
	v_cmp_ne_u32_e32 vcc, 0, v12
	s_cbranch_vccz .Lsc_s5
	s_nop 0
	v_mbcnt_lo_u32_b32 v13, vcc_lo, 0
	v_mbcnt_hi_u32_b32 v13, vcc_hi, v13
	v_add_u32_e32 v13, s42, v13
	v_cmp_gt_i32_e64 s[0:1], s7, v13
	s_and_b64 s[4:5], vcc, s[0:1]
	s_and_saveexec_b64 s[0:1], s[4:5]
	v_lshl_add_u32 v14, v13, 4, v9
	v_lshl_add_u32 v15, v13, 2, v10
	v_add_u32_e32 v13, 0x500, v8
	ds_write_b128 v14, v[20:23]
	ds_write_b32 v15, v13
	s_mov_b64 exec, -1
	s_bcnt1_i32_b64 s40, vcc
	s_add_i32 s42, s42, s40
.Lsc_s5:
	s_waitcnt lgkmcnt(0)
	s_add_u32 m0, s6, 0x1800
	s_add_u32 s40, s38, 0x6800
	buffer_load_dwordx4 v2, s[28:31], s40 offen nt lds
	s_waitcnt vmcnt(19)
	ds_read_b128 v[20:23], v24 offset:7168
	v_or3_b32 v12, v16, v17, v18
	v_bitop3_b32 v12, v12, s9, v19 bitop3:0xc8
	v_cmp_ne_u32_e32 vcc, 0, v12
	s_cbranch_vccz .Lsc_s6
	s_nop 0
	v_mbcnt_lo_u32_b32 v13, vcc_lo, 0
	v_mbcnt_hi_u32_b32 v13, vcc_hi, v13
	v_add_u32_e32 v13, s42, v13
	v_cmp_gt_i32_e64 s[0:1], s7, v13
	s_and_b64 s[4:5], vcc, s[0:1]
	s_and_saveexec_b64 s[0:1], s[4:5]
	v_lshl_add_u32 v14, v13, 4, v9
	v_lshl_add_u32 v15, v13, 2, v10
	v_add_u32_e32 v13, 0x600, v8
	ds_write_b128 v14, v[16:19]
	ds_write_b32 v15, v13
	s_mov_b64 exec, -1
	s_bcnt1_i32_b64 s40, vcc
	s_add_i32 s42, s42, s40
.Lsc_s6:
	s_waitcnt lgkmcnt(0)
	s_add_u32 m0, s6, 0x1c00
	s_add_u32 s40, s38, 0x6c00
	buffer_load_dwordx4 v2, s[28:31], s40 offen nt lds
	s_waitcnt vmcnt(19)
	ds_read_b128 v[16:19], v24 offset:8192
	v_or3_b32 v12, v20, v21, v22
	v_bitop3_b32 v12, v12, s9, v23 bitop3:0xc8
	v_cmp_ne_u32_e32 vcc, 0, v12
	s_cbranch_vccz .Lsc_s7
	s_nop 0
	v_mbcnt_lo_u32_b32 v13, vcc_lo, 0
	v_mbcnt_hi_u32_b32 v13, vcc_hi, v13
	v_add_u32_e32 v13, s42, v13
	v_cmp_gt_i32_e64 s[0:1], s7, v13
	s_and_b64 s[4:5], vcc, s[0:1]
	s_and_saveexec_b64 s[0:1], s[4:5]
	v_lshl_add_u32 v14, v13, 4, v9
	v_lshl_add_u32 v15, v13, 2, v10
	v_add_u32_e32 v13, 0x700, v8
	ds_write_b128 v14, v[20:23]
	ds_write_b32 v15, v13
	s_mov_b64 exec, -1
	s_bcnt1_i32_b64 s40, vcc
	s_add_i32 s42, s42, s40
.Lsc_s7:
	s_waitcnt lgkmcnt(0)
	s_add_u32 m0, s6, 0x2000
	s_add_u32 s40, s38, 0x7000
	buffer_load_dwordx4 v2, s[28:31], s40 offen nt lds
	s_waitcnt vmcnt(19)
	ds_read_b128 v[20:23], v24 offset:9216
	v_or3_b32 v12, v16, v17, v18
	v_bitop3_b32 v12, v12, s9, v19 bitop3:0xc8
	v_cmp_ne_u32_e32 vcc, 0, v12
	s_cbranch_vccz .Lsc_s8
	s_nop 0
	v_mbcnt_lo_u32_b32 v13, vcc_lo, 0
	v_mbcnt_hi_u32_b32 v13, vcc_hi, v13
	v_add_u32_e32 v13, s42, v13
	v_cmp_gt_i32_e64 s[0:1], s7, v13
	s_and_b64 s[4:5], vcc, s[0:1]
	s_and_saveexec_b64 s[0:1], s[4:5]
	v_lshl_add_u32 v14, v13, 4, v9
	v_lshl_add_u32 v15, v13, 2, v10
	v_add_u32_e32 v13, 0x800, v8
	ds_write_b128 v14, v[16:19]
	ds_write_b32 v15, v13
	s_mov_b64 exec, -1
	s_bcnt1_i32_b64 s40, vcc
	s_add_i32 s42, s42, s40
.Lsc_s8:
	s_waitcnt lgkmcnt(0)
	s_add_u32 m0, s6, 0x2400
	s_add_u32 s40, s38, 0x7400
	buffer_load_dwordx4 v2, s[28:31], s40 offen nt lds
	s_waitcnt vmcnt(19)
	ds_read_b128 v[16:19], v24 offset:10240
	v_or3_b32 v12, v20, v21, v22
	v_bitop3_b32 v12, v12, s9, v23 bitop3:0xc8
	v_cmp_ne_u32_e32 vcc, 0, v12
	s_cbranch_vccz .Lsc_s9
	s_nop 0
	v_mbcnt_lo_u32_b32 v13, vcc_lo, 0
	v_mbcnt_hi_u32_b32 v13, vcc_hi, v13
	v_add_u32_e32 v13, s42, v13
	v_cmp_gt_i32_e64 s[0:1], s7, v13
	s_and_b64 s[4:5], vcc, s[0:1]
	s_and_saveexec_b64 s[0:1], s[4:5]
	v_lshl_add_u32 v14, v13, 4, v9
	v_lshl_add_u32 v15, v13, 2, v10
	v_add_u32_e32 v13, 0x900, v8
	ds_write_b128 v14, v[20:23]
	ds_write_b32 v15, v13
	s_mov_b64 exec, -1
	s_bcnt1_i32_b64 s40, vcc
	s_add_i32 s42, s42, s40
.Lsc_s9:
	s_waitcnt lgkmcnt(0)
	s_add_u32 m0, s6, 0x2800
	s_add_u32 s40, s38, 0x7800
	buffer_load_dwordx4 v2, s[28:31], s40 offen nt lds
	s_waitcnt vmcnt(19)
	ds_read_b128 v[20:23], v24 offset:11264
	v_or3_b32 v12, v16, v17, v18
	v_bitop3_b32 v12, v12, s9, v19 bitop3:0xc8
	v_cmp_ne_u32_e32 vcc, 0, v12
	s_cbranch_vccz .Lsc_s10
	s_nop 0
	v_mbcnt_lo_u32_b32 v13, vcc_lo, 0
	v_mbcnt_hi_u32_b32 v13, vcc_hi, v13
	v_add_u32_e32 v13, s42, v13
	v_cmp_gt_i32_e64 s[0:1], s7, v13
	s_and_b64 s[4:5], vcc, s[0:1]
	s_and_saveexec_b64 s[0:1], s[4:5]
	v_lshl_add_u32 v14, v13, 4, v9
	v_lshl_add_u32 v15, v13, 2, v10
	v_add_u32_e32 v13, 0xa00, v8
	ds_write_b128 v14, v[16:19]
	ds_write_b32 v15, v13
	s_mov_b64 exec, -1
	s_bcnt1_i32_b64 s40, vcc
	s_add_i32 s42, s42, s40
.Lsc_s10:
	s_waitcnt lgkmcnt(0)
	s_add_u32 m0, s6, 0x2c00
	s_add_u32 s40, s38, 0x7c00
	buffer_load_dwordx4 v2, s[28:31], s40 offen nt lds
	s_waitcnt vmcnt(19)
	ds_read_b128 v[16:19], v24 offset:12288
	v_or3_b32 v12, v20, v21, v22
	v_bitop3_b32 v12, v12, s9, v23 bitop3:0xc8
	v_cmp_ne_u32_e32 vcc, 0, v12
	s_cbranch_vccz .Lsc_s11
	s_nop 0
	v_mbcnt_lo_u32_b32 v13, vcc_lo, 0
	v_mbcnt_hi_u32_b32 v13, vcc_hi, v13
	v_add_u32_e32 v13, s42, v13
	v_cmp_gt_i32_e64 s[0:1], s7, v13
	s_and_b64 s[4:5], vcc, s[0:1]
	s_and_saveexec_b64 s[0:1], s[4:5]
	v_lshl_add_u32 v14, v13, 4, v9
	v_lshl_add_u32 v15, v13, 2, v10
	v_add_u32_e32 v13, 0xb00, v8
	ds_write_b128 v14, v[20:23]
	ds_write_b32 v15, v13
	s_mov_b64 exec, -1
	s_bcnt1_i32_b64 s40, vcc
	s_add_i32 s42, s42, s40
.Lsc_s11:
	s_waitcnt lgkmcnt(0)
	s_add_u32 m0, s6, 0x3000
	s_add_u32 s40, s38, 0x8000
	buffer_load_dwordx4 v2, s[28:31], s40 offen nt lds
	s_waitcnt vmcnt(19)
	ds_read_b128 v[20:23], v24 offset:13312
	v_or3_b32 v12, v16, v17, v18
	v_bitop3_b32 v12, v12, s9, v19 bitop3:0xc8
	v_cmp_ne_u32_e32 vcc, 0, v12
	s_cbranch_vccz .Lsc_s12
	s_nop 0
	v_mbcnt_lo_u32_b32 v13, vcc_lo, 0
	v_mbcnt_hi_u32_b32 v13, vcc_hi, v13
	v_add_u32_e32 v13, s42, v13
	v_cmp_gt_i32_e64 s[0:1], s7, v13
	s_and_b64 s[4:5], vcc, s[0:1]
	s_and_saveexec_b64 s[0:1], s[4:5]
	v_lshl_add_u32 v14, v13, 4, v9
	v_lshl_add_u32 v15, v13, 2, v10
	v_add_u32_e32 v13, 0xc00, v8
	ds_write_b128 v14, v[16:19]
	ds_write_b32 v15, v13
	s_mov_b64 exec, -1
	s_bcnt1_i32_b64 s40, vcc
	s_add_i32 s42, s42, s40
.Lsc_s12:
	s_waitcnt lgkmcnt(0)
	s_add_u32 m0, s6, 0x3400
	s_add_u32 s40, s38, 0x8400
	buffer_load_dwordx4 v2, s[28:31], s40 offen nt lds
	s_waitcnt vmcnt(19)
	ds_read_b128 v[16:19], v24 offset:14336
	v_or3_b32 v12, v20, v21, v22
	v_bitop3_b32 v12, v12, s9, v23 bitop3:0xc8
	v_cmp_ne_u32_e32 vcc, 0, v12
	s_cbranch_vccz .Lsc_s13
	s_nop 0
	v_mbcnt_lo_u32_b32 v13, vcc_lo, 0
	v_mbcnt_hi_u32_b32 v13, vcc_hi, v13
	v_add_u32_e32 v13, s42, v13
	v_cmp_gt_i32_e64 s[0:1], s7, v13
	s_and_b64 s[4:5], vcc, s[0:1]
	s_and_saveexec_b64 s[0:1], s[4:5]
	v_lshl_add_u32 v14, v13, 4, v9
	v_lshl_add_u32 v15, v13, 2, v10
	v_add_u32_e32 v13, 0xd00, v8
	ds_write_b128 v14, v[20:23]
	ds_write_b32 v15, v13
	s_mov_b64 exec, -1
	s_bcnt1_i32_b64 s40, vcc
	s_add_i32 s42, s42, s40
.Lsc_s13:
	s_waitcnt lgkmcnt(0)
	s_add_u32 m0, s6, 0x3800
	s_add_u32 s40, s38, 0x8800
	buffer_load_dwordx4 v2, s[28:31], s40 offen nt lds
	s_waitcnt vmcnt(19)
	ds_read_b128 v[20:23], v24 offset:15360
	v_or3_b32 v12, v16, v17, v18
	v_bitop3_b32 v12, v12, s9, v19 bitop3:0xc8
	v_cmp_ne_u32_e32 vcc, 0, v12
	s_cbranch_vccz .Lsc_s14
	s_nop 0
	v_mbcnt_lo_u32_b32 v13, vcc_lo, 0
	v_mbcnt_hi_u32_b32 v13, vcc_hi, v13
	v_add_u32_e32 v13, s42, v13
	v_cmp_gt_i32_e64 s[0:1], s7, v13
	s_and_b64 s[4:5], vcc, s[0:1]
	s_and_saveexec_b64 s[0:1], s[4:5]
	v_lshl_add_u32 v14, v13, 4, v9
	v_lshl_add_u32 v15, v13, 2, v10
	v_add_u32_e32 v13, 0xe00, v8
	ds_write_b128 v14, v[16:19]
	ds_write_b32 v15, v13
	s_mov_b64 exec, -1
	s_bcnt1_i32_b64 s40, vcc
	s_add_i32 s42, s42, s40
.Lsc_s14:
	s_waitcnt lgkmcnt(0)
	s_add_u32 m0, s6, 0x3c00
	s_add_u32 s40, s38, 0x8c00
	buffer_load_dwordx4 v2, s[28:31], s40 offen nt lds
	s_waitcnt vmcnt(19)
	ds_read_b128 v[16:19], v24 offset:16384
	v_or3_b32 v12, v20, v21, v22
	v_bitop3_b32 v12, v12, s9, v23 bitop3:0xc8
	v_cmp_ne_u32_e32 vcc, 0, v12
	s_cbranch_vccz .Lsc_s15
	s_nop 0
	v_mbcnt_lo_u32_b32 v13, vcc_lo, 0
	v_mbcnt_hi_u32_b32 v13, vcc_hi, v13
	v_add_u32_e32 v13, s42, v13
	v_cmp_gt_i32_e64 s[0:1], s7, v13
	s_and_b64 s[4:5], vcc, s[0:1]
	s_and_saveexec_b64 s[0:1], s[4:5]
	v_lshl_add_u32 v14, v13, 4, v9
	v_lshl_add_u32 v15, v13, 2, v10
	v_add_u32_e32 v13, 0xf00, v8
	ds_write_b128 v14, v[20:23]
	ds_write_b32 v15, v13
	s_mov_b64 exec, -1
	s_bcnt1_i32_b64 s40, vcc
	s_add_i32 s42, s42, s40
.Lsc_s15:
	s_waitcnt lgkmcnt(0)
	s_add_u32 m0, s6, 0x4000
	s_add_u32 s40, s38, 0x9000
	buffer_load_dwordx4 v2, s[28:31], s40 offen nt lds
	s_waitcnt vmcnt(19)
	ds_read_b128 v[20:23], v24 offset:17408
	v_or3_b32 v12, v16, v17, v18
	v_bitop3_b32 v12, v12, s9, v19 bitop3:0xc8
	v_cmp_ne_u32_e32 vcc, 0, v12
	s_cbranch_vccz .Lsc_s16
	s_nop 0
	v_mbcnt_lo_u32_b32 v13, vcc_lo, 0
	v_mbcnt_hi_u32_b32 v13, vcc_hi, v13
	v_add_u32_e32 v13, s42, v13
	v_cmp_gt_i32_e64 s[0:1], s7, v13
	s_and_b64 s[4:5], vcc, s[0:1]
	s_and_saveexec_b64 s[0:1], s[4:5]
	v_lshl_add_u32 v14, v13, 4, v9
	v_lshl_add_u32 v15, v13, 2, v10
	v_add_u32_e32 v13, 0x1000, v8
	ds_write_b128 v14, v[16:19]
	ds_write_b32 v15, v13
	s_mov_b64 exec, -1
	s_bcnt1_i32_b64 s40, vcc
	s_add_i32 s42, s42, s40
.Lsc_s16:
	s_waitcnt lgkmcnt(0)
	s_add_u32 m0, s6, 0x4400
	s_add_u32 s40, s38, 0x9400
	buffer_load_dwordx4 v2, s[28:31], s40 offen nt lds
	s_waitcnt vmcnt(19)
	ds_read_b128 v[16:19], v24 offset:18432
	v_or3_b32 v12, v20, v21, v22
	v_bitop3_b32 v12, v12, s9, v23 bitop3:0xc8
	v_cmp_ne_u32_e32 vcc, 0, v12
	s_cbranch_vccz .Lsc_s17
	s_nop 0
	v_mbcnt_lo_u32_b32 v13, vcc_lo, 0
	v_mbcnt_hi_u32_b32 v13, vcc_hi, v13
	v_add_u32_e32 v13, s42, v13
	v_cmp_gt_i32_e64 s[0:1], s7, v13
	s_and_b64 s[4:5], vcc, s[0:1]
	s_and_saveexec_b64 s[0:1], s[4:5]
	v_lshl_add_u32 v14, v13, 4, v9
	v_lshl_add_u32 v15, v13, 2, v10
	v_add_u32_e32 v13, 0x1100, v8
	ds_write_b128 v14, v[20:23]
	ds_write_b32 v15, v13
	s_mov_b64 exec, -1
	s_bcnt1_i32_b64 s40, vcc
	s_add_i32 s42, s42, s40
.Lsc_s17:
	s_waitcnt lgkmcnt(0)
	s_add_u32 m0, s6, 0x4800
	s_add_u32 s40, s38, 0x9800
	buffer_load_dwordx4 v2, s[28:31], s40 offen nt lds
	s_waitcnt vmcnt(19)
	ds_read_b128 v[20:23], v24 offset:19456
	v_or3_b32 v12, v16, v17, v18
	v_bitop3_b32 v12, v12, s9, v19 bitop3:0xc8
	v_cmp_ne_u32_e32 vcc, 0, v12
	s_cbranch_vccz .Lsc_s18
	s_nop 0
	v_mbcnt_lo_u32_b32 v13, vcc_lo, 0
	v_mbcnt_hi_u32_b32 v13, vcc_hi, v13
	v_add_u32_e32 v13, s42, v13
	v_cmp_gt_i32_e64 s[0:1], s7, v13
	s_and_b64 s[4:5], vcc, s[0:1]
	s_and_saveexec_b64 s[0:1], s[4:5]
	v_lshl_add_u32 v14, v13, 4, v9
	v_lshl_add_u32 v15, v13, 2, v10
	v_add_u32_e32 v13, 0x1200, v8
	ds_write_b128 v14, v[16:19]
	ds_write_b32 v15, v13
	s_mov_b64 exec, -1
	s_bcnt1_i32_b64 s40, vcc
	s_add_i32 s42, s42, s40
.Lsc_s18:
	s_waitcnt lgkmcnt(0)
	s_add_u32 m0, s6, 0x4c00
	s_add_u32 s40, s38, 0x9c00
	buffer_load_dwordx4 v4, s[28:31], s40 offen nt lds
	s_waitcnt vmcnt(19)
	ds_read_b128 v[16:19], v24
	v_or3_b32 v12, v20, v21, v22
	v_bitop3_b32 v12, v12, s9, v23 bitop3:0xc8
	v_cmp_ne_u32_e32 vcc, 0, v12
	s_cbranch_vccz .Lsc_s19
	s_nop 0
	v_mbcnt_lo_u32_b32 v13, vcc_lo, 0
	v_mbcnt_hi_u32_b32 v13, vcc_hi, v13
	v_add_u32_e32 v13, s42, v13
	v_cmp_gt_i32_e64 s[0:1], s7, v13
	s_and_b64 s[4:5], vcc, s[0:1]
	s_and_saveexec_b64 s[0:1], s[4:5]
	v_lshl_add_u32 v14, v13, 4, v9
	v_lshl_add_u32 v15, v13, 2, v10
	v_add_u32_e32 v13, 0x1300, v8
	ds_write_b128 v14, v[20:23]
	ds_write_b32 v15, v13
	s_mov_b64 exec, -1
	s_bcnt1_i32_b64 s40, vcc
	s_add_i32 s42, s42, s40
.Lsc_s19:
	s_waitcnt lgkmcnt(0)
	s_mov_b32 m0, s6
	s_mov_b32 s40, s39
	buffer_load_dwordx4 v5, s[28:31], s40 offen nt lds
	s_waitcnt vmcnt(19)
	ds_read_b128 v[20:23], v24 offset:1024
	v_or3_b32 v12, v16, v17, v18
	v_bitop3_b32 v12, v12, s9, v19 bitop3:0xc8
	v_cmp_ne_u32_e32 vcc, 0, v12
	s_cbranch_vccz .Lsc_s20
	s_nop 0
	v_mbcnt_lo_u32_b32 v13, vcc_lo, 0
	v_mbcnt_hi_u32_b32 v13, vcc_hi, v13
	v_add_u32_e32 v13, s42, v13
	v_cmp_gt_i32_e64 s[0:1], s7, v13
	s_and_b64 s[4:5], vcc, s[0:1]
	s_and_saveexec_b64 s[0:1], s[4:5]
	v_lshl_add_u32 v14, v13, 4, v9
	v_lshl_add_u32 v15, v13, 2, v10
	v_add_u32_e32 v13, 0x1400, v8
	ds_write_b128 v14, v[16:19]
	ds_write_b32 v15, v13
	s_mov_b64 exec, -1
	s_bcnt1_i32_b64 s40, vcc
	s_add_i32 s42, s42, s40
.Lsc_s20:
	s_waitcnt lgkmcnt(0)
	s_add_u32 m0, s6, 0x400
	s_add_u32 s40, s39, 0x400
	buffer_load_dwordx4 v6, s[28:31], s40 offen nt lds
	s_waitcnt vmcnt(19)
	ds_read_b128 v[16:19], v24 offset:2048
	v_or3_b32 v12, v20, v21, v22
	v_bitop3_b32 v12, v12, s9, v23 bitop3:0xc8
	v_cmp_ne_u32_e32 vcc, 0, v12
	s_cbranch_vccz .Lsc_s21
	s_nop 0
	v_mbcnt_lo_u32_b32 v13, vcc_lo, 0
	v_mbcnt_hi_u32_b32 v13, vcc_hi, v13
	v_add_u32_e32 v13, s42, v13
	v_cmp_gt_i32_e64 s[0:1], s7, v13
	s_and_b64 s[4:5], vcc, s[0:1]
	s_and_saveexec_b64 s[0:1], s[4:5]
	v_lshl_add_u32 v14, v13, 4, v9
	v_lshl_add_u32 v15, v13, 2, v10
	v_add_u32_e32 v13, 0x1500, v8
	ds_write_b128 v14, v[20:23]
	ds_write_b32 v15, v13
	s_mov_b64 exec, -1
	s_bcnt1_i32_b64 s40, vcc
	s_add_i32 s42, s42, s40
.Lsc_s21:
	s_waitcnt lgkmcnt(0)
	s_add_u32 m0, s6, 0x800
	s_add_u32 s40, s39, 0x800
	buffer_load_dwordx4 v6, s[28:31], s40 offen nt lds
	s_waitcnt vmcnt(19)
	ds_read_b128 v[20:23], v24 offset:3072
	v_or3_b32 v12, v16, v17, v18
	v_bitop3_b32 v12, v12, s9, v19 bitop3:0xc8
	v_cmp_ne_u32_e32 vcc, 0, v12
	s_cbranch_vccz .Lsc_s22
	s_nop 0
	v_mbcnt_lo_u32_b32 v13, vcc_lo, 0
	v_mbcnt_hi_u32_b32 v13, vcc_hi, v13
	v_add_u32_e32 v13, s42, v13
	v_cmp_gt_i32_e64 s[0:1], s7, v13
	s_and_b64 s[4:5], vcc, s[0:1]
	s_and_saveexec_b64 s[0:1], s[4:5]
	v_lshl_add_u32 v14, v13, 4, v9
	v_lshl_add_u32 v15, v13, 2, v10
	v_add_u32_e32 v13, 0x1600, v8
	ds_write_b128 v14, v[16:19]
	ds_write_b32 v15, v13
	s_mov_b64 exec, -1
	s_bcnt1_i32_b64 s40, vcc
	s_add_i32 s42, s42, s40
.Lsc_s22:
	s_waitcnt lgkmcnt(0)
	s_add_u32 m0, s6, 0xc00
	s_add_u32 s40, s39, 0xc00
	buffer_load_dwordx4 v6, s[28:31], s40 offen nt lds
	s_waitcnt vmcnt(19)
	ds_read_b128 v[16:19], v24 offset:4096
	v_or3_b32 v12, v20, v21, v22
	v_bitop3_b32 v12, v12, s9, v23 bitop3:0xc8
	v_cmp_ne_u32_e32 vcc, 0, v12
	s_cbranch_vccz .Lsc_s23
	s_nop 0
	v_mbcnt_lo_u32_b32 v13, vcc_lo, 0
	v_mbcnt_hi_u32_b32 v13, vcc_hi, v13
	v_add_u32_e32 v13, s42, v13
	v_cmp_gt_i32_e64 s[0:1], s7, v13
	s_and_b64 s[4:5], vcc, s[0:1]
	s_and_saveexec_b64 s[0:1], s[4:5]
	v_lshl_add_u32 v14, v13, 4, v9
	v_lshl_add_u32 v15, v13, 2, v10
	v_add_u32_e32 v13, 0x1700, v8
	ds_write_b128 v14, v[20:23]
	ds_write_b32 v15, v13
	s_mov_b64 exec, -1
	s_bcnt1_i32_b64 s40, vcc
	s_add_i32 s42, s42, s40
.Lsc_s23:
	s_waitcnt lgkmcnt(0)
	s_add_u32 m0, s6, 0x1000
	s_add_u32 s40, s39, 0x1000
	buffer_load_dwordx4 v6, s[28:31], s40 offen nt lds
	s_waitcnt vmcnt(19)
	ds_read_b128 v[20:23], v24 offset:5120
	v_or3_b32 v12, v16, v17, v18
	v_bitop3_b32 v12, v12, s9, v19 bitop3:0xc8
	v_cmp_ne_u32_e32 vcc, 0, v12
	s_cbranch_vccz .Lsc_s24
	s_nop 0
	v_mbcnt_lo_u32_b32 v13, vcc_lo, 0
	v_mbcnt_hi_u32_b32 v13, vcc_hi, v13
	v_add_u32_e32 v13, s42, v13
	v_cmp_gt_i32_e64 s[0:1], s7, v13
	s_and_b64 s[4:5], vcc, s[0:1]
	s_and_saveexec_b64 s[0:1], s[4:5]
	v_lshl_add_u32 v14, v13, 4, v9
	v_lshl_add_u32 v15, v13, 2, v10
	v_add_u32_e32 v13, 0x1800, v8
	ds_write_b128 v14, v[16:19]
	ds_write_b32 v15, v13
	s_mov_b64 exec, -1
	s_bcnt1_i32_b64 s40, vcc
	s_add_i32 s42, s42, s40
.Lsc_s24:
	s_waitcnt lgkmcnt(0)
	s_add_u32 m0, s6, 0x1400
	s_add_u32 s40, s39, 0x1400
	buffer_load_dwordx4 v6, s[28:31], s40 offen nt lds
	s_waitcnt vmcnt(19)
	ds_read_b128 v[16:19], v24 offset:6144
	v_or3_b32 v12, v20, v21, v22
	v_bitop3_b32 v12, v12, s9, v23 bitop3:0xc8
	v_cmp_ne_u32_e32 vcc, 0, v12
	s_cbranch_vccz .Lsc_s25
	s_nop 0
	v_mbcnt_lo_u32_b32 v13, vcc_lo, 0
	v_mbcnt_hi_u32_b32 v13, vcc_hi, v13
	v_add_u32_e32 v13, s42, v13
	v_cmp_gt_i32_e64 s[0:1], s7, v13
	s_and_b64 s[4:5], vcc, s[0:1]
	s_and_saveexec_b64 s[0:1], s[4:5]
	v_lshl_add_u32 v14, v13, 4, v9
	v_lshl_add_u32 v15, v13, 2, v10
	v_add_u32_e32 v13, 0x1900, v8
	ds_write_b128 v14, v[20:23]
	ds_write_b32 v15, v13
	s_mov_b64 exec, -1
	s_bcnt1_i32_b64 s40, vcc
	s_add_i32 s42, s42, s40
.Lsc_s25:
	s_waitcnt lgkmcnt(0)
	s_add_u32 m0, s6, 0x1800
	s_add_u32 s40, s39, 0x1800
	buffer_load_dwordx4 v6, s[28:31], s40 offen nt lds
	s_waitcnt vmcnt(19)
	ds_read_b128 v[20:23], v24 offset:7168
	v_or3_b32 v12, v16, v17, v18
	v_bitop3_b32 v12, v12, s9, v19 bitop3:0xc8
	v_cmp_ne_u32_e32 vcc, 0, v12
	s_cbranch_vccz .Lsc_s26
	s_nop 0
	v_mbcnt_lo_u32_b32 v13, vcc_lo, 0
	v_mbcnt_hi_u32_b32 v13, vcc_hi, v13
	v_add_u32_e32 v13, s42, v13
	v_cmp_gt_i32_e64 s[0:1], s7, v13
	s_and_b64 s[4:5], vcc, s[0:1]
	s_and_saveexec_b64 s[0:1], s[4:5]
	v_lshl_add_u32 v14, v13, 4, v9
	v_lshl_add_u32 v15, v13, 2, v10
	v_add_u32_e32 v13, 0x1a00, v8
	ds_write_b128 v14, v[16:19]
	ds_write_b32 v15, v13
	s_mov_b64 exec, -1
	s_bcnt1_i32_b64 s40, vcc
	s_add_i32 s42, s42, s40
.Lsc_s26:
	s_waitcnt lgkmcnt(0)
	s_add_u32 m0, s6, 0x1c00
	s_add_u32 s40, s39, 0x1c00
	buffer_load_dwordx4 v6, s[28:31], s40 offen nt lds
	s_waitcnt vmcnt(19)
	ds_read_b128 v[16:19], v24 offset:8192
	v_or3_b32 v12, v20, v21, v22
	v_bitop3_b32 v12, v12, s9, v23 bitop3:0xc8
	v_cmp_ne_u32_e32 vcc, 0, v12
	s_cbranch_vccz .Lsc_s27
	s_nop 0
	v_mbcnt_lo_u32_b32 v13, vcc_lo, 0
	v_mbcnt_hi_u32_b32 v13, vcc_hi, v13
	v_add_u32_e32 v13, s42, v13
	v_cmp_gt_i32_e64 s[0:1], s7, v13
	s_and_b64 s[4:5], vcc, s[0:1]
	s_and_saveexec_b64 s[0:1], s[4:5]
	v_lshl_add_u32 v14, v13, 4, v9
	v_lshl_add_u32 v15, v13, 2, v10
	v_add_u32_e32 v13, 0x1b00, v8
	ds_write_b128 v14, v[20:23]
	ds_write_b32 v15, v13
	s_mov_b64 exec, -1
	s_bcnt1_i32_b64 s40, vcc
	s_add_i32 s42, s42, s40
.Lsc_s27:
	s_waitcnt lgkmcnt(0)
	s_add_u32 m0, s6, 0x2000
	s_add_u32 s40, s39, 0x2000
	buffer_load_dwordx4 v6, s[28:31], s40 offen nt lds
	s_waitcnt vmcnt(19)
	ds_read_b128 v[20:23], v24 offset:9216
	v_or3_b32 v12, v16, v17, v18
	v_bitop3_b32 v12, v12, s9, v19 bitop3:0xc8
	v_cmp_ne_u32_e32 vcc, 0, v12
	s_cbranch_vccz .Lsc_s28
	s_nop 0
	v_mbcnt_lo_u32_b32 v13, vcc_lo, 0
	v_mbcnt_hi_u32_b32 v13, vcc_hi, v13
	v_add_u32_e32 v13, s42, v13
	v_cmp_gt_i32_e64 s[0:1], s7, v13
	s_and_b64 s[4:5], vcc, s[0:1]
	s_and_saveexec_b64 s[0:1], s[4:5]
	v_lshl_add_u32 v14, v13, 4, v9
	v_lshl_add_u32 v15, v13, 2, v10
	v_add_u32_e32 v13, 0x1c00, v8
	ds_write_b128 v14, v[16:19]
	ds_write_b32 v15, v13
	s_mov_b64 exec, -1
	s_bcnt1_i32_b64 s40, vcc
	s_add_i32 s42, s42, s40
.Lsc_s28:
	s_waitcnt lgkmcnt(0)
	s_add_u32 m0, s6, 0x2400
	s_add_u32 s40, s39, 0x2400
	buffer_load_dwordx4 v6, s[28:31], s40 offen nt lds
	s_waitcnt vmcnt(19)
	ds_read_b128 v[16:19], v24 offset:10240
	v_or3_b32 v12, v20, v21, v22
	v_bitop3_b32 v12, v12, s9, v23 bitop3:0xc8
	v_cmp_ne_u32_e32 vcc, 0, v12
	s_cbranch_vccz .Lsc_s29
	s_nop 0
	v_mbcnt_lo_u32_b32 v13, vcc_lo, 0
	v_mbcnt_hi_u32_b32 v13, vcc_hi, v13
	v_add_u32_e32 v13, s42, v13
	v_cmp_gt_i32_e64 s[0:1], s7, v13
	s_and_b64 s[4:5], vcc, s[0:1]
	s_and_saveexec_b64 s[0:1], s[4:5]
	v_lshl_add_u32 v14, v13, 4, v9
	v_lshl_add_u32 v15, v13, 2, v10
	v_add_u32_e32 v13, 0x1d00, v8
	ds_write_b128 v14, v[20:23]
	ds_write_b32 v15, v13
	s_mov_b64 exec, -1
	s_bcnt1_i32_b64 s40, vcc
	s_add_i32 s42, s42, s40
.Lsc_s29:
	s_waitcnt lgkmcnt(0)
	s_add_u32 m0, s6, 0x2800
	s_add_u32 s40, s39, 0x2800
	buffer_load_dwordx4 v6, s[28:31], s40 offen nt lds
	s_waitcnt vmcnt(19)
	ds_read_b128 v[20:23], v24 offset:11264
	v_or3_b32 v12, v16, v17, v18
	v_bitop3_b32 v12, v12, s9, v19 bitop3:0xc8
	v_cmp_ne_u32_e32 vcc, 0, v12
	s_cbranch_vccz .Lsc_s30
	s_nop 0
	v_mbcnt_lo_u32_b32 v13, vcc_lo, 0
	v_mbcnt_hi_u32_b32 v13, vcc_hi, v13
	v_add_u32_e32 v13, s42, v13
	v_cmp_gt_i32_e64 s[0:1], s7, v13
	s_and_b64 s[4:5], vcc, s[0:1]
	s_and_saveexec_b64 s[0:1], s[4:5]
	v_lshl_add_u32 v14, v13, 4, v9
	v_lshl_add_u32 v15, v13, 2, v10
	v_add_u32_e32 v13, 0x1e00, v8
	ds_write_b128 v14, v[16:19]
	ds_write_b32 v15, v13
	s_mov_b64 exec, -1
	s_bcnt1_i32_b64 s40, vcc
	s_add_i32 s42, s42, s40
.Lsc_s30:
	s_waitcnt lgkmcnt(0)
	s_add_u32 m0, s6, 0x2c00
	s_add_u32 s40, s39, 0x2c00
	buffer_load_dwordx4 v6, s[28:31], s40 offen nt lds
	s_waitcnt vmcnt(19)
	ds_read_b128 v[16:19], v24 offset:12288
	v_or3_b32 v12, v20, v21, v22
	v_bitop3_b32 v12, v12, s9, v23 bitop3:0xc8
	v_cmp_ne_u32_e32 vcc, 0, v12
	s_cbranch_vccz .Lsc_s31
	s_nop 0
	v_mbcnt_lo_u32_b32 v13, vcc_lo, 0
	v_mbcnt_hi_u32_b32 v13, vcc_hi, v13
	v_add_u32_e32 v13, s42, v13
	v_cmp_gt_i32_e64 s[0:1], s7, v13
	s_and_b64 s[4:5], vcc, s[0:1]
	s_and_saveexec_b64 s[0:1], s[4:5]
	v_lshl_add_u32 v14, v13, 4, v9
	v_lshl_add_u32 v15, v13, 2, v10
	v_add_u32_e32 v13, 0x1f00, v8
	ds_write_b128 v14, v[20:23]
	ds_write_b32 v15, v13
	s_mov_b64 exec, -1
	s_bcnt1_i32_b64 s40, vcc
	s_add_i32 s42, s42, s40
.Lsc_s31:
	s_waitcnt lgkmcnt(0)
	s_add_u32 m0, s6, 0x3000
	s_add_u32 s40, s39, 0x3000
	buffer_load_dwordx4 v6, s[28:31], s40 offen nt lds
	s_waitcnt vmcnt(19)
	ds_read_b128 v[20:23], v24 offset:13312
	v_or3_b32 v12, v16, v17, v18
	v_bitop3_b32 v12, v12, s9, v19 bitop3:0xc8
	v_cmp_ne_u32_e32 vcc, 0, v12
	s_cbranch_vccz .Lsc_s32
	s_nop 0
	v_mbcnt_lo_u32_b32 v13, vcc_lo, 0
	v_mbcnt_hi_u32_b32 v13, vcc_hi, v13
	v_add_u32_e32 v13, s42, v13
	v_cmp_gt_i32_e64 s[0:1], s7, v13
	s_and_b64 s[4:5], vcc, s[0:1]
	s_and_saveexec_b64 s[0:1], s[4:5]
	v_lshl_add_u32 v14, v13, 4, v9
	v_lshl_add_u32 v15, v13, 2, v10
	v_add_u32_e32 v13, 0x2000, v8
	ds_write_b128 v14, v[16:19]
	ds_write_b32 v15, v13
	s_mov_b64 exec, -1
	s_bcnt1_i32_b64 s40, vcc
	s_add_i32 s42, s42, s40
.Lsc_s32:
	s_waitcnt lgkmcnt(0)
	s_add_u32 m0, s6, 0x3400
	s_add_u32 s40, s39, 0x3400
	buffer_load_dwordx4 v6, s[28:31], s40 offen nt lds
	s_waitcnt vmcnt(19)
	ds_read_b128 v[16:19], v24 offset:14336
	v_or3_b32 v12, v20, v21, v22
	v_bitop3_b32 v12, v12, s9, v23 bitop3:0xc8
	v_cmp_ne_u32_e32 vcc, 0, v12
	s_cbranch_vccz .Lsc_s33
	s_nop 0
	v_mbcnt_lo_u32_b32 v13, vcc_lo, 0
	v_mbcnt_hi_u32_b32 v13, vcc_hi, v13
	v_add_u32_e32 v13, s42, v13
	v_cmp_gt_i32_e64 s[0:1], s7, v13
	s_and_b64 s[4:5], vcc, s[0:1]
	s_and_saveexec_b64 s[0:1], s[4:5]
	v_lshl_add_u32 v14, v13, 4, v9
	v_lshl_add_u32 v15, v13, 2, v10
	v_add_u32_e32 v13, 0x2100, v8
	ds_write_b128 v14, v[20:23]
	ds_write_b32 v15, v13
	s_mov_b64 exec, -1
	s_bcnt1_i32_b64 s40, vcc
	s_add_i32 s42, s42, s40
.Lsc_s33:
	s_waitcnt lgkmcnt(0)
	s_add_u32 m0, s6, 0x3800
	s_add_u32 s40, s39, 0x3800
	buffer_load_dwordx4 v6, s[28:31], s40 offen nt lds
	s_waitcnt vmcnt(19)
	ds_read_b128 v[20:23], v24 offset:15360
	v_or3_b32 v12, v16, v17, v18
	v_bitop3_b32 v12, v12, s9, v19 bitop3:0xc8
	v_cmp_ne_u32_e32 vcc, 0, v12
	s_cbranch_vccz .Lsc_s34
	s_nop 0
	v_mbcnt_lo_u32_b32 v13, vcc_lo, 0
	v_mbcnt_hi_u32_b32 v13, vcc_hi, v13
	v_add_u32_e32 v13, s42, v13
	v_cmp_gt_i32_e64 s[0:1], s7, v13
	s_and_b64 s[4:5], vcc, s[0:1]
	s_and_saveexec_b64 s[0:1], s[4:5]
	v_lshl_add_u32 v14, v13, 4, v9
	v_lshl_add_u32 v15, v13, 2, v10
	v_add_u32_e32 v13, 0x2200, v8
	ds_write_b128 v14, v[16:19]
	ds_write_b32 v15, v13
	s_mov_b64 exec, -1
	s_bcnt1_i32_b64 s40, vcc
	s_add_i32 s42, s42, s40
.Lsc_s34:
	s_waitcnt lgkmcnt(0)
	s_add_u32 m0, s6, 0x3c00
	s_add_u32 s40, s39, 0x3c00
	buffer_load_dwordx4 v6, s[28:31], s40 offen nt lds
	s_waitcnt vmcnt(19)
	ds_read_b128 v[16:19], v24 offset:16384
	v_or3_b32 v12, v20, v21, v22
	v_bitop3_b32 v12, v12, s9, v23 bitop3:0xc8
	v_cmp_ne_u32_e32 vcc, 0, v12
	s_cbranch_vccz .Lsc_s35
	s_nop 0
	v_mbcnt_lo_u32_b32 v13, vcc_lo, 0
	v_mbcnt_hi_u32_b32 v13, vcc_hi, v13
	v_add_u32_e32 v13, s42, v13
	v_cmp_gt_i32_e64 s[0:1], s7, v13
	s_and_b64 s[4:5], vcc, s[0:1]
	s_and_saveexec_b64 s[0:1], s[4:5]
	v_lshl_add_u32 v14, v13, 4, v9
	v_lshl_add_u32 v15, v13, 2, v10
	v_add_u32_e32 v13, 0x2300, v8
	ds_write_b128 v14, v[20:23]
	ds_write_b32 v15, v13
	s_mov_b64 exec, -1
	s_bcnt1_i32_b64 s40, vcc
	s_add_i32 s42, s42, s40
.Lsc_s35:
	s_waitcnt lgkmcnt(0)
	s_add_u32 m0, s6, 0x4000
	s_add_u32 s40, s39, 0x4000
	buffer_load_dwordx4 v6, s[28:31], s40 offen nt lds
	s_waitcnt vmcnt(19)
	ds_read_b128 v[20:23], v24 offset:17408
	v_or3_b32 v12, v16, v17, v18
	v_bitop3_b32 v12, v12, s9, v19 bitop3:0xc8
	v_cmp_ne_u32_e32 vcc, 0, v12
	s_cbranch_vccz .Lsc_s36
	s_nop 0
	v_mbcnt_lo_u32_b32 v13, vcc_lo, 0
	v_mbcnt_hi_u32_b32 v13, vcc_hi, v13
	v_add_u32_e32 v13, s42, v13
	v_cmp_gt_i32_e64 s[0:1], s7, v13
	s_and_b64 s[4:5], vcc, s[0:1]
	s_and_saveexec_b64 s[0:1], s[4:5]
	v_lshl_add_u32 v14, v13, 4, v9
	v_lshl_add_u32 v15, v13, 2, v10
	v_add_u32_e32 v13, 0x2400, v8
	ds_write_b128 v14, v[16:19]
	ds_write_b32 v15, v13
	s_mov_b64 exec, -1
	s_bcnt1_i32_b64 s40, vcc
	s_add_i32 s42, s42, s40
.Lsc_s36:
	s_waitcnt lgkmcnt(0)
	s_add_u32 m0, s6, 0x4400
	s_add_u32 s40, s39, 0x4400
	buffer_load_dwordx4 v6, s[28:31], s40 offen nt lds
	s_waitcnt vmcnt(19)
	ds_read_b128 v[16:19], v24 offset:18432
	v_or3_b32 v12, v20, v21, v22
	v_bitop3_b32 v12, v12, s9, v23 bitop3:0xc8
	v_cmp_ne_u32_e32 vcc, 0, v12
	s_cbranch_vccz .Lsc_s37
	s_nop 0
	v_mbcnt_lo_u32_b32 v13, vcc_lo, 0
	v_mbcnt_hi_u32_b32 v13, vcc_hi, v13
	v_add_u32_e32 v13, s42, v13
	v_cmp_gt_i32_e64 s[0:1], s7, v13
	s_and_b64 s[4:5], vcc, s[0:1]
	s_and_saveexec_b64 s[0:1], s[4:5]
	v_lshl_add_u32 v14, v13, 4, v9
	v_lshl_add_u32 v15, v13, 2, v10
	v_add_u32_e32 v13, 0x2500, v8
	ds_write_b128 v14, v[20:23]
	ds_write_b32 v15, v13
	s_mov_b64 exec, -1
	s_bcnt1_i32_b64 s40, vcc
	s_add_i32 s42, s42, s40
.Lsc_s37:
	s_waitcnt lgkmcnt(0)
	s_add_u32 m0, s6, 0x4800
	s_add_u32 s40, s39, 0x4800
	buffer_load_dwordx4 v6, s[28:31], s40 offen nt lds
	s_waitcnt vmcnt(19)
	ds_read_b128 v[20:23], v24 offset:19456
	v_or3_b32 v12, v16, v17, v18
	v_bitop3_b32 v12, v12, s9, v19 bitop3:0xc8
	v_cmp_ne_u32_e32 vcc, 0, v12
	s_cbranch_vccz .Lsc_s38
	s_nop 0
	v_mbcnt_lo_u32_b32 v13, vcc_lo, 0
	v_mbcnt_hi_u32_b32 v13, vcc_hi, v13
	v_add_u32_e32 v13, s42, v13
	v_cmp_gt_i32_e64 s[0:1], s7, v13
	s_and_b64 s[4:5], vcc, s[0:1]
	s_and_saveexec_b64 s[0:1], s[4:5]
	v_lshl_add_u32 v14, v13, 4, v9
	v_lshl_add_u32 v15, v13, 2, v10
	v_add_u32_e32 v13, 0x2600, v8
	ds_write_b128 v14, v[16:19]
	ds_write_b32 v15, v13
	s_mov_b64 exec, -1
	s_bcnt1_i32_b64 s40, vcc
	s_add_i32 s42, s42, s40
.Lsc_s38:
	s_waitcnt lgkmcnt(0)
	s_add_u32 m0, s6, 0x4c00
	s_add_u32 s40, s39, 0x4c00
	buffer_load_dwordx4 v6, s[28:31], s40 offen nt lds
	s_waitcnt vmcnt(19)
	ds_read_b128 v[16:19], v24
	v_or3_b32 v12, v20, v21, v22
	v_bitop3_b32 v12, v12, s9, v23 bitop3:0xc8
	v_cmp_ne_u32_e32 vcc, 0, v12
	s_and_b64 vcc, vcc, s[50:51]
	s_cbranch_vccz .Lsc_s39
	s_nop 0
	v_mbcnt_lo_u32_b32 v13, vcc_lo, 0
	v_mbcnt_hi_u32_b32 v13, vcc_hi, v13
	v_add_u32_e32 v13, s42, v13
	v_cmp_gt_i32_e64 s[0:1], s7, v13
	s_and_b64 s[4:5], vcc, s[0:1]
	s_and_saveexec_b64 s[0:1], s[4:5]
	v_lshl_add_u32 v14, v13, 4, v9
	v_lshl_add_u32 v15, v13, 2, v10
	v_add_u32_e32 v13, 0x2700, v8
	ds_write_b128 v14, v[20:23]
	ds_write_b32 v15, v13
	s_mov_b64 exec, -1
	s_bcnt1_i32_b64 s40, vcc
	s_add_i32 s42, s42, s40
.Lsc_s39:
	s_waitcnt lgkmcnt(0)
	s_add_i32 s42, s42, 1
	v_mov_b32_e32 v12, s42
	ds_write_b32 v11, v12
	s_cmp_eq_u32 s35, s36
	s_cbranch_scc1 .LBB1_384
	s_add_i32 s35, s35, 1
	s_mov_b32 s37, s52
	s_mov_b32 s38, s39
	s_mov_b32 s47, s53
	s_branch .Lsc_row

	.amdhsa_kernel _Z11attn_kernelPKfS0_PKDv8_DF16_S0_Pfi
		.amdhsa_group_segment_fixed_size 119808
		.amdhsa_private_segment_fixed_size 0
		.amdhsa_kernarg_size 44
		.amdhsa_user_sgpr_count 2
		.amdhsa_user_sgpr_dispatch_ptr 0
		.amdhsa_user_sgpr_queue_ptr 0
		.amdhsa_user_sgpr_kernarg_segment_ptr 1
		.amdhsa_user_sgpr_dispatch_id 0
		.amdhsa_user_sgpr_kernarg_preload_length 0
		.amdhsa_user_sgpr_kernarg_preload_offset 0
		.amdhsa_user_sgpr_private_segment_size 0
		.amdhsa_uses_dynamic_stack 0
		.amdhsa_enable_private_segment 0
		.amdhsa_system_sgpr_workgroup_id_x 1
		.amdhsa_system_sgpr_workgroup_id_y 0
		.amdhsa_system_sgpr_workgroup_id_z 0
		.amdhsa_system_sgpr_workgroup_info 0
		.amdhsa_system_vgpr_workitem_id 0
		.amdhsa_next_free_vgpr 248
		.amdhsa_next_free_sgpr 54
		.amdhsa_accum_offset 248
		.amdhsa_reserve_vcc 1
		.amdhsa_float_round_mode_32 0
		.amdhsa_float_round_mode_16_64 0
		.amdhsa_float_denorm_mode_32 3
		.amdhsa_float_denorm_mode_16_64 3
		.amdhsa_dx10_clamp 1
		.amdhsa_ieee_mode 1
		.amdhsa_fp16_overflow 0
		.amdhsa_tg_split 0
		.amdhsa_exception_fp_ieee_invalid_op 0
		.amdhsa_exception_fp_denorm_src 0
		.amdhsa_exception_fp_ieee_div_zero 0
		.amdhsa_exception_fp_ieee_overflow 0
		.amdhsa_exception_fp_ieee_underflow 0
		.amdhsa_exception_fp_ieee_inexact 0
		.amdhsa_exception_int_div_zero 0
	.end_amdhsa_kernel

amdhsa.kernels:
  - .agpr_count:     0
    .args:
      - .actual_access:  read_only
        .address_space:  global
        .offset:         0
        .size:           8
        .value_kind:     global_buffer
      - .actual_access:  read_only
        .address_space:  global
        .offset:         8
        .size:           8
        .value_kind:     global_buffer
      - .actual_access:  write_only
        .address_space:  global
        .offset:         16
        .size:           8
        .value_kind:     global_buffer
      - .actual_access:  write_only
        .address_space:  global
        .offset:         24
        .size:           8
        .value_kind:     global_buffer
      - .offset:         32
        .size:           4
        .value_kind:     hidden_block_count_x
      - .offset:         36
        .size:           4
        .value_kind:     hidden_block_count_y
      - .offset:         40
        .size:           4
        .value_kind:     hidden_block_count_z
      - .offset:         44
        .size:           2
        .value_kind:     hidden_group_size_x
      - .offset:         46
        .size:           2
        .value_kind:     hidden_group_size_y
      - .offset:         48
        .size:           2
        .value_kind:     hidden_group_size_z
      - .offset:         50
        .size:           2
        .value_kind:     hidden_remainder_x
      - .offset:         52
        .size:           2
        .value_kind:     hidden_remainder_y
      - .offset:         54
        .size:           2
        .value_kind:     hidden_remainder_z
      - .offset:         72
        .size:           8
        .value_kind:     hidden_global_offset_x
      - .offset:         80
        .size:           8
        .value_kind:     hidden_global_offset_y
      - .offset:         88
        .size:           8
        .value_kind:     hidden_global_offset_z
      - .offset:         96
        .size:           2
        .value_kind:     hidden_grid_dims
    .group_segment_fixed_size: 0
    .kernarg_segment_align: 8
    .kernarg_segment_size: 288
    .language:       OpenCL C
    .language_version:
      - 2
      - 0
    .max_flat_workgroup_size: 256
    .name:           _Z11prep_kernelPKfS0_PfPDv4_DF16_
    .private_segment_fixed_size: 0
    .sgpr_count:     20
    .sgpr_spill_count: 0
    .symbol:         _Z11prep_kernelPKfS0_PfPDv4_DF16_.kd
    .uniform_work_group_size: 1
    .uses_dynamic_stack: false
    .vgpr_count:     17
    .vgpr_spill_count: 0
    .wavefront_size: 64
  - .agpr_count:     0
    .args:
      - .actual_access:  read_only
        .address_space:  global
        .offset:         0
        .size:           8
        .value_kind:     global_buffer
      - .actual_access:  read_only
        .address_space:  global
        .offset:         8
        .size:           8
        .value_kind:     global_buffer
      - .actual_access:  read_only
        .address_space:  global
        .offset:         16
        .size:           8
        .value_kind:     global_buffer
      - .actual_access:  read_only
        .address_space:  global
        .offset:         24
        .size:           8
        .value_kind:     global_buffer
      - .actual_access:  write_only
        .address_space:  global
        .offset:         32
        .size:           8
        .value_kind:     global_buffer
      - .offset:         40
        .size:           4
        .value_kind:     by_value
    .group_segment_fixed_size: 119808
    .kernarg_segment_align: 8
    .kernarg_segment_size: 44
    .language:       OpenCL C
    .language_version:
      - 2
      - 0
    .max_flat_workgroup_size: 512
    .name:           _Z11attn_kernelPKfS0_PKDv8_DF16_S0_Pfi
    .private_segment_fixed_size: 0
    .sgpr_count:     60
    .sgpr_spill_count: 0
    .symbol:         _Z11attn_kernelPKfS0_PKDv8_DF16_S0_Pfi.kd
    .uniform_work_group_size: 1
    .uses_dynamic_stack: false
    .vgpr_count:     248
    .vgpr_spill_count: 0
    .wavefront_size: 64
